# mLSTM state pass: per-chunk state store (LDS transpose + global stores) moved behind the half-step barrier so the barrier's vmcnt(0) does not wait for it; on top of nacc-pipelined stack
# baseline (speedup 1.0000x reference)
; #define LAS __attribute__((address_space(3)))
; template <int DK, int DVB, bool MLSTM>
; __device__ __forceinline__ void state_unit2(LAS unsigned char* lds, LAS unsigned char* ldstab, const StateArgs a, const int wv) {
;     ...
;         const int ci = hs >> 1, half = hs & 1, c = a.dir ? 31 - ci : ci, t0 = c * 128;
;         LAS float* wt = wtab + (ci & 1) * 128;
;         if (half == 0) {
;             bf16_t* co = a.Cout + (size_t)c * a.cstride + (size_t)(32 * dkb) * a.ldc + 32 * dvb0;
;             if constexpr (BPW == 4) { store_blocks_t<2>(ts, lane, acc, co, a.ldc); store_blocks_t<2>(ts, lane, acc + 2, co + 64, a.ldc); }
;             else store_blocks_t<1>(ts, lane, acc, co, a.ldc);
;             if (MLSTM) { if (a.Nout && tid < DK) a.Nout[(size_t)c * DK + tid] = nacc; }
;             if (MLSTM) { const float F = a.alpha[t0 + (a.dir ? 0 : 127)];
;                 if (tid < 128) wt[tid] = __expf(F - a.alpha[t0 + tid] + a.beta[t0 + tid] - a.Mseq);
;                 eF = __expf(F);
.LBB0_555:
	s_lshl_b32 s6, s69, 8
	s_and_b32 s6, s6, 0x200
	s_add_i32 s73, s6, 0
	s_lshr_b32 s70, s69, 1
	s_and_b32 s72, s69, 1
	s_add_i32 s73, s73, 0x21500
	s_cmp_eq_u32 s72, 0
	s_cselect_b64 s[6:7], -1, 0
	s_cmp_eq_u32 s72, 1
	s_cselect_b64 s[40:41], -1, 0
	s_and_b64 vcc, exec, s[40:41]
	s_cbranch_vccnz .LBB0_561
	s_sub_i32 s8, 31, s70
	s_and_b64 s[40:41], s[26:27], exec
	s_cselect_b32 s8, s70, s8
	s_lshl_b32 s71, s8, 7
	s_or_b32 s8, s71, s68
	s_lshl_b64 s[40:41], s[8:9], 2
	s_add_u32 s40, s16, s40
	s_addc_u32 s41, s17, s41
	global_load_dword v35, v17, s[40:41]
	s_and_saveexec_b64 s[40:41], s[4:5]
	s_cbranch_execz .LBB0_560
	v_add_u32_e32 v62, s71, v18
	v_ashrrev_i32_e32 v63, 31, v62
	v_lshlrev_b64 v[62:63], 2, v[62:63]
	v_lshl_add_u64 v[64:65], s[16:17], 0, v[62:63]
	v_lshl_add_u64 v[62:63], s[24:25], 0, v[62:63]
	global_load_dword v37, v[64:65], off
	global_load_dword v39, v[62:63], off
	s_waitcnt vmcnt(0)
	v_sub_f32_e32 v37, v35, v37
	v_add_f32_e32 v37, v37, v39
	v_sub_f32_e32 v37, v37, v46
	v_mul_f32_e32 v37, 0x3fb8aa3b, v37
	v_exp_f32_e32 v37, v37
	v_lshl_add_u32 v39, v18, 2, s73
	ds_write_b32 v39, v37

; #define LAS __attribute__((address_space(3)))
; #define LDS_WAIT() asm volatile("s_waitcnt lgkmcnt(0)" ::: "memory")
; __device__ __forceinline__ bf16_t f2bf(float f) { unsigned u = __builtin_bit_cast(unsigned, f); return (bf16_t)((u + 0x7fffu + ((u >> 16) & 1u)) >> 16); }
; __device__ __forceinline__ int crow(int r, int hi) { return (r & 3) + 8 * (r >> 2) + 4 * hi; }
; __device__ __forceinline__ int crow(int r, int hi) { return (r & 3) + 8 * (r >> 2) + 4 * hi; }
; template <int NBLK>
; __device__ __forceinline__ void store_blocks_t(LAS unsigned char* ts, int lane, const f32x16* blk, bf16_t* dst, int ldd) {
;     constexpr int RB = 64 * NBLK;
;     const int r32 = lane & 31, hi = lane >> 5;
; #pragma unroll
;     for (int j = 0; j < NBLK; ++j)
; #pragma unroll
;         for (int r = 0; r < 16; ++r) *(LAS bf16_t*)(ts + crow(r, hi) * RB + (32 * j + r32) * 2) = f2bf(blk[j][r]);
;     LDS_WAIT();
;     constexpr int CPR = 4 * NBLK, NCH = 32 * CPR;
; #pragma unroll
;     for (int it = 0; it < NCH / 64; ++it) { const int id = it * 64 + lane, row = id / CPR, ch = id % CPR;
;         *(u32x4*)(dst + (size_t)row * ldd + 8 * ch) = *(const LAS u32x4*)(ts + row * RB + ch * 16); }
;     LDS_WAIT();
; template <int DK, int DVB, bool MLSTM>
; __device__ __forceinline__ void state_unit2(LAS unsigned char* lds, LAS unsigned char* ldstab, const StateArgs a, const int wv) {
;     ...
;         if (half == 0) {
; #pragma unroll
;             for (int j = 0; j < BPW; ++j)
; #pragma unroll
;                 for (int r = 0; r < 16; ++r) acc[j][r] *= eF;
.LBB0_563:
	s_andn2_b64 vcc, exec, s[6:7]
	s_cbranch_vccnz .LBB0_565
	v_bfe_u32 v35, v0, 16, 1
	v_add3_u32 v35, v0, v35, s62
	ds_write_b16_d16_hi v53, v35
	v_bfe_u32 v35, v1, 16, 1
	v_add3_u32 v35, v1, v35, s62
	ds_write_b16_d16_hi v53, v35 offset:64
	v_bfe_u32 v35, v2, 16, 1
	v_add3_u32 v35, v2, v35, s62
	ds_write_b16_d16_hi v53, v35 offset:128
	v_bfe_u32 v35, v3, 16, 1
	v_add3_u32 v35, v3, v35, s62
	ds_write_b16_d16_hi v54, v35
	v_bfe_u32 v35, v4, 16, 1
	v_add3_u32 v35, v4, v35, s62
	ds_write_b16_d16_hi v53, v35 offset:512
	v_bfe_u32 v35, v5, 16, 1
	v_add3_u32 v35, v5, v35, s62
	ds_write_b16_d16_hi v53, v35 offset:576
	v_bfe_u32 v35, v6, 16, 1
	v_add3_u32 v35, v6, v35, s62
	ds_write_b16_d16_hi v53, v35 offset:640
	v_bfe_u32 v35, v7, 16, 1
	v_add3_u32 v35, v7, v35, s62
	ds_write_b16_d16_hi v55, v35
	v_bfe_u32 v35, v8, 16, 1
	v_add3_u32 v35, v8, v35, s62
	ds_write_b16_d16_hi v53, v35 offset:1024
	v_bfe_u32 v35, v9, 16, 1
	v_add3_u32 v35, v9, v35, s62
	ds_write_b16_d16_hi v53, v35 offset:1088
	v_bfe_u32 v35, v10, 16, 1
	v_add3_u32 v35, v10, v35, s62
	ds_write_b16_d16_hi v53, v35 offset:1152
	v_bfe_u32 v35, v11, 16, 1
	v_add3_u32 v35, v11, v35, s62
	ds_write_b16_d16_hi v56, v35
	v_bfe_u32 v35, v12, 16, 1
	v_add3_u32 v35, v12, v35, s62
	ds_write_b16_d16_hi v53, v35 offset:1536
	v_bfe_u32 v35, v13, 16, 1
	v_add3_u32 v35, v13, v35, s62
	ds_write_b16_d16_hi v53, v35 offset:1600
	v_bfe_u32 v35, v14, 16, 1
	v_add3_u32 v35, v14, v35, s62
	ds_write_b16_d16_hi v53, v35 offset:1664
	v_bfe_u32 v35, v15, 16, 1
	v_add3_u32 v35, v15, v35, s62
	ds_write_b16_d16_hi v57, v35
	s_sub_i32 s8, 31, s70
	s_waitcnt lgkmcnt(0)
	s_and_b64 s[40:41], s[26:27], exec
	ds_read_b128 v[62:65], v58
	ds_read_b128 v[66:69], v59
	s_cselect_b32 s8, s70, s8
	s_lshl_b64 s[40:41], s[8:9], 15
	v_lshl_add_u64 v[70:71], v[30:31], 0, s[40:41]
	v_lshl_add_u64 v[72:73], v[70:71], 0, v[16:17]
	v_mov_b32_e32 v35, v17
	s_waitcnt lgkmcnt(0)
	global_store_dwordx4 v[72:73], v[62:65], off
	s_nop 1
	v_lshl_add_u64 v[62:63], v[70:71], 0, v[34:35]
	global_store_dwordx4 v[62:63], v[66:69], off
	s_waitcnt lgkmcnt(0)
	s_and_saveexec_b64 s[40:41], s[36:37]
	s_cbranch_execz .Lstmv_558
	s_lshl_b64 s[74:75], s[8:9], 9
	v_lshl_add_u64 v[62:63], v[32:33], 0, s[74:75]
	global_store_dword v[62:63], v60, off
.Lstmv_558:
	s_or_b64 exec, exec, s[40:41]
	v_pk_mul_f32 v[14:15], v[14:15], v[44:45] op_sel_hi:[1,0]
	v_pk_mul_f32 v[12:13], v[12:13], v[44:45] op_sel_hi:[1,0]
	v_pk_mul_f32 v[10:11], v[10:11], v[44:45] op_sel_hi:[1,0]
	v_pk_mul_f32 v[8:9], v[8:9], v[44:45] op_sel_hi:[1,0]
	v_pk_mul_f32 v[6:7], v[6:7], v[44:45] op_sel_hi:[1,0]
	v_pk_mul_f32 v[4:5], v[4:5], v[44:45] op_sel_hi:[1,0]
	v_pk_mul_f32 v[2:3], v[2:3], v[44:45] op_sel_hi:[1,0]
	v_pk_mul_f32 v[0:1], v[0:1], v[44:45] op_sel_hi:[1,0]
